# v16
# baseline (speedup 1.0000x reference)
_Z8k_layer1PKiS0_PKfS2_PK15HIP_vector_typeIjLj4EEPKDv8_DF16_S9_S2_S2_S2_PDF16_PfSB_:
	s_load_dwordx2 s[14:15], s[0:1], 0x48
	s_load_dwordx8 s[4:11], s[0:1], 0x28
	v_readfirstlane_b32 s13, v0
	s_lshr_b32 s12, s13, 6
	v_and_b32_e32 v178, 63, v0
	v_lshl_or_b32 v2, s12, 10, v178
	v_ashrrev_i32_e32 v3, 31, v2
	v_lshlrev_b64 v[4:5], 4, v[2:3]
	s_waitcnt lgkmcnt(0)
	v_lshl_add_u64 v[6:7], s[6:7], 0, v[4:5]
	s_movk_i32 s3, 0x1000
	v_add_co_u32_e32 v8, vcc, s3, v6
	s_movk_i32 s6, 0x2000
	s_nop 0
	v_addc_co_u32_e32 v9, vcc, 0, v7, vcc
	v_add_co_u32_e32 v10, vcc, s6, v6
	s_movk_i32 s6, 0x3000
	s_nop 0
	v_addc_co_u32_e32 v11, vcc, 0, v7, vcc
	global_load_dwordx4 v[32:35], v[6:7], off
	global_load_dwordx4 v[36:39], v[6:7], off offset:1024
	global_load_dwordx4 v[40:43], v[6:7], off offset:2048
	global_load_dwordx4 v[44:47], v[6:7], off offset:3072
	v_add_co_u32_e32 v6, vcc, s6, v6
	v_lshl_add_u64 v[4:5], s[4:5], 0, v[4:5]
	s_nop 0
	v_addc_co_u32_e32 v7, vcc, 0, v7, vcc
	v_or_b32_e32 v2, 0x200, v2
	global_load_dwordx4 v[48:51], v[8:9], off offset:1024
	global_load_dwordx4 v[52:55], v[8:9], off offset:2048
	global_load_dwordx4 v[56:59], v[10:11], off offset:-4096
	global_load_dwordx4 v[60:63], v[10:11], off
	global_load_dwordx4 v[64:67], v[10:11], off offset:1024
	global_load_dwordx4 v[68:71], v[10:11], off offset:2048
	global_load_dwordx4 v[72:75], v[10:11], off offset:3072
	global_load_dwordx4 v[76:79], v[8:9], off offset:3072
	global_load_dwordx4 v[80:83], v[6:7], off
	global_load_dwordx4 v[84:87], v[6:7], off offset:1024
	global_load_dwordx4 v[88:91], v[6:7], off offset:2048
	global_load_dwordx4 v[92:95], v[6:7], off offset:3072
	v_add_co_u32_e32 v6, vcc, s3, v4
	v_ashrrev_i32_e32 v3, 31, v2
	s_nop 0
	v_addc_co_u32_e32 v7, vcc, 0, v5, vcc
	v_lshl_add_u64 v[2:3], v[2:3], 4, s[4:5]
	global_load_dwordx4 v[96:99], v[4:5], off
	global_load_dwordx4 v[100:103], v[4:5], off offset:1024
	global_load_dwordx4 v[104:107], v[4:5], off offset:2048
	global_load_dwordx4 v[108:111], v[4:5], off offset:3072
	global_load_dwordx4 v[112:115], v[6:7], off
	global_load_dwordx4 v[116:119], v[6:7], off offset:1024
	global_load_dwordx4 v[120:123], v[6:7], off offset:2048
	global_load_dwordx4 v[124:127], v[6:7], off offset:3072
	global_load_dwordx4 v[128:131], v[2:3], off
	global_load_dwordx4 v[132:135], v[2:3], off offset:1024
	global_load_dwordx4 v[136:139], v[2:3], off offset:2048
	global_load_dwordx4 v[140:143], v[2:3], off offset:3072
	v_add_co_u32_e32 v2, vcc, s6, v4
	s_lshl_b32 s3, s12, 4
	s_nop 0
	v_addc_co_u32_e32 v3, vcc, 0, v5, vcc
	global_load_dwordx4 v[144:147], v[2:3], off
	global_load_dwordx4 v[148:151], v[2:3], off offset:1024
	global_load_dwordx4 v[152:155], v[2:3], off offset:2048
	global_load_dwordx4 v[156:159], v[2:3], off offset:3072
	v_and_or_b32 v1, v0, 15, s3
	v_lshlrev_b32_e32 v1, 2, v1
	global_load_dword v179, v1, s[10:11]
	global_load_dword v180, v1, s[14:15]
	v_bfe_u32 v2, v0, 4, 2
	s_lshl_b32 s16, s3, 2
	v_lshl_add_u32 v2, v2, 4, s16
	global_load_dwordx4 v[228:231], v2, s[10:11]
	global_load_dwordx4 v[232:235], v2, s[14:15]
	v_cmp_gt_u32_e32 vcc, 32, v0
	v_lshlrev_b32_e32 v0, 2, v0
	s_and_saveexec_b64 s[4:5], vcc
	v_mov_b32_e32 v1, 0
	v_add_u32_e32 v2, 0xd000, v0
	ds_write2_b32 v2, v1, v1 offset0:176 offset1:208
	s_or_b64 exec, exec, s[4:5]
	global_load_dword v1, v0, s[8:9]
	global_load_dword v2, v0, s[8:9] offset:1024
	s_cmpk_gt_i32 s2, 0x61a
	s_waitcnt vmcnt(0)
	ds_write2st64_b32 v0, v1, v2 offset0:202 offset1:206
	s_waitcnt lgkmcnt(0)
	s_barrier
	s_cbranch_scc1 .LBB3_271
	s_load_dwordx8 s[56:63], s[0:1], 0x0
	s_load_dwordx4 s[4:7], s[0:1], 0x50
	s_mul_i32 s87, s12, 48
	s_lshl_b32 s66, s12, 9
	s_and_b32 s65, s13, 0xffffffc0
	s_lshl_b32 s86, s12, 3
	s_waitcnt lgkmcnt(0)
	v_writelane_b32 v226, s4, 0
	s_add_i32 s87, s87, 0xd200
	s_add_i32 s90, s66, 0xc200
	v_writelane_b32 v226, s5, 1
	v_writelane_b32 v226, s6, 2
	v_writelane_b32 v226, s7, 3
	s_lshl_b32 s4, s12, 12
	s_add_i32 s88, s4, 0x8200
	s_lshl_b32 s5, s12, 1
	s_load_dwordx2 s[72:73], s[0:1], 0x20
	s_load_dwordx2 s[76:77], s[0:1], 0x60
	s_add_u32 s0, s0, 0x68
	s_addc_u32 s1, s1, 0
	v_mbcnt_lo_u32_b32 v0, -1, 0
	v_writelane_b32 v226, s0, 4
	v_mbcnt_hi_u32_b32 v182, -1, v0
	s_mul_i32 s99, s12, 0x2080
	v_writelane_b32 v226, s1, 5
	s_or_b32 s0, s5, 1
	v_and_b32_e32 v0, 64, v182
	s_mov_b32 s91, 0xff800000
	s_lshl_b32 s95, s12, 8
	s_lshl_b32 s64, s0, 8
	s_lshl_b32 s98, s0, 7
	s_add_i32 s93, s4, 0x8500
	s_or_b32 s92, s99, 48
	s_mov_b32 s68, 0
	v_mov_b32_e32 v177, 0
	v_mov_b32_e32 v181, 0xff800000
	s_movk_i32 s69, 0x410
	v_xor_b32_e32 v183, 32, v182
	v_add_u32_e32 v184, 64, v0
	v_xor_b32_e32 v185, 4, v182
	v_xor_b32_e32 v186, 8, v182
	v_xor_b32_e32 v187, 16, v182
	v_mov_b32_e32 v188, 0x3c0
	v_writelane_b32 v226, s92, 6
	s_branch .LBB3_6

.LBB3_222:
	v_lshlrev_b32_e32 v0, 4, v168
	v_add_u32_e32 v165, 0xca00, v0
	v_mad_u32_u24 v166, v167, s69, v0
	v_add_u32_e32 v12, s66, v165
	s_waitcnt lgkmcnt(0)
	s_barrier
	ds_read_b128 v[16:19], v12
	ds_read_b128 v[20:23], v12 offset:32
	ds_read_b128 v[24:27], v12 offset:64
	ds_read_b128 v[28:31], v12 offset:96
	v_add_u32_e32 v169, s95, v166
	ds_read_b128 v[160:163], v169
	ds_read_b128 v[170:173], v169 offset:32
	s_waitcnt lgkmcnt(1)
	v_mfma_f32_32x32x16_f16 v[16:31], v[96:99], v[160:163], v[16:31]
	ds_read_b128 v[0:3], v12 offset:128
	ds_read_b128 v[4:7], v12 offset:160
	ds_read_b128 v[8:11], v12 offset:192
	ds_read_b128 v[12:15], v12 offset:224
	v_lshlrev_b32_e32 v168, 3, v168
	v_mad_u32_u24 v174, v167, s69, v168
	v_add_u32_e32 v167, s95, v174
	s_mov_b32 s8, 0xc34f
	s_waitcnt lgkmcnt(4)
	v_mfma_f32_32x32x16_f16 v[16:31], v[100:103], v[170:173], v[16:31]
	s_waitcnt lgkmcnt(0)
	v_mfma_f32_32x32x16_f16 v[0:15], v[112:115], v[160:163], v[0:15]
	ds_read_b128 v[160:163], v169 offset:64
	ds_read_b128 v[190:193], v169 offset:96
	s_waitcnt lgkmcnt(1)
	v_mfma_f32_32x32x16_f16 v[16:31], v[104:107], v[160:163], v[16:31]
	v_mfma_f32_32x32x16_f16 v[0:15], v[116:119], v[170:173], v[0:15]
	s_waitcnt lgkmcnt(0)
	v_mfma_f32_32x32x16_f16 v[16:31], v[108:111], v[190:193], v[16:31]
	v_mfma_f32_32x32x16_f16 v[0:15], v[120:123], v[160:163], v[0:15]
	s_nop 10
	v_max_f32_e32 v17, v17, v17
	v_max_f32_e32 v18, v18, v18
	v_max_f32_e32 v19, v19, v19
	v_max_f32_e32 v16, v16, v16
	v_max_f32_e32 v20, v20, v20
	v_max_f32_e32 v21, v21, v21
	v_max_f32_e32 v22, v22, v22
	v_max_f32_e32 v168, 0, v17
	v_max_f32_e32 v17, 0, v18
	v_max_f32_e32 v18, 0, v19
	v_max_f32_e32 v19, v23, v23
	v_max_f32_e32 v16, 0, v16
	v_max_f32_e32 v20, 0, v20
	v_max_f32_e32 v21, 0, v21
	v_cvt_pk_f16_f32 v17, v17, v18
	v_max_f32_e32 v18, 0, v22
	v_max_f32_e32 v19, 0, v19
	v_mfma_f32_32x32x16_f16 v[0:15], v[124:127], v[190:193], v[0:15]
	v_cvt_pk_f16_f32 v16, v16, v168
	v_cvt_pk_f16_f32 v19, v18, v19
	v_cvt_pk_f16_f32 v18, v20, v21
	ds_write2_b64 v167, v[16:17], v[18:19] offset1:2
	v_max_f32_e32 v17, v25, v25
	v_max_f32_e32 v18, 0, v17
	v_max_f32_e32 v17, v26, v26
	v_max_f32_e32 v19, v27, v27
	v_max_f32_e32 v16, v24, v24
	v_max_f32_e32 v17, 0, v17
	v_max_f32_e32 v19, 0, v19
	v_max_f32_e32 v16, 0, v16
	v_cvt_pk_f16_f32 v17, v17, v19
	v_max_f32_e32 v19, v29, v29
	v_cvt_pk_f16_f32 v16, v16, v18
	v_max_f32_e32 v18, v28, v28
	v_max_f32_e32 v20, 0, v19
	v_max_f32_e32 v19, v30, v30
	v_max_f32_e32 v21, v31, v31
	v_max_f32_e32 v18, 0, v18
	v_max_f32_e32 v19, 0, v19
	v_max_f32_e32 v21, 0, v21
	v_cvt_pk_f16_f32 v19, v19, v21
	v_cvt_pk_f16_f32 v18, v18, v20
	v_max_f32_e32 v1, v1, v1
	ds_write2_b64 v167, v[16:17], v[18:19] offset0:4 offset1:6
	v_max_f32_e32 v16, 0, v1
	v_max_f32_e32 v1, v2, v2
	v_max_f32_e32 v2, v3, v3
	v_max_f32_e32 v1, 0, v1
	v_max_f32_e32 v2, 0, v2
	v_max_f32_e32 v3, v5, v5
	v_max_f32_e32 v0, v0, v0
	v_cvt_pk_f16_f32 v1, v1, v2
	v_max_f32_e32 v2, v4, v4
	v_max_f32_e32 v4, 0, v3
	v_max_f32_e32 v3, v6, v6
	v_max_f32_e32 v5, v7, v7
	v_max_f32_e32 v0, 0, v0
	v_max_f32_e32 v2, 0, v2
	v_max_f32_e32 v3, 0, v3
	v_max_f32_e32 v5, 0, v5
	v_cvt_pk_f16_f32 v0, v0, v16
	v_cvt_pk_f16_f32 v3, v3, v5
	v_cvt_pk_f16_f32 v2, v2, v4
	ds_write2_b64 v167, v[0:1], v[2:3] offset0:8 offset1:10
	v_max_f32_e32 v1, v9, v9
	v_max_f32_e32 v2, 0, v1
	v_max_f32_e32 v1, v10, v10
	v_max_f32_e32 v3, v11, v11
	v_max_f32_e32 v0, v8, v8
	v_max_f32_e32 v1, 0, v1
	v_max_f32_e32 v3, 0, v3
	v_max_f32_e32 v0, 0, v0
	v_cvt_pk_f16_f32 v1, v1, v3
	v_max_f32_e32 v3, v13, v13
	v_cvt_pk_f16_f32 v0, v0, v2
	v_max_f32_e32 v2, v12, v12
	v_max_f32_e32 v4, 0, v3
	v_max_f32_e32 v3, v14, v14
	v_max_f32_e32 v5, v15, v15
	v_max_f32_e32 v2, 0, v2
	v_max_f32_e32 v3, 0, v3
	v_max_f32_e32 v5, 0, v5
	v_cvt_pk_f16_f32 v3, v3, v5
	v_cvt_pk_f16_f32 v2, v2, v4
	ds_write2_b64 v167, v[0:1], v[2:3] offset0:12 offset1:14
	v_add_u32_e32 v12, s64, v165
	ds_read_b128 v[16:19], v12
	ds_read_b128 v[20:23], v12 offset:32
	ds_read_b128 v[24:27], v12 offset:64
	ds_read_b128 v[28:31], v12 offset:96
	v_add_u32_e32 v165, s98, v166
	ds_read_b128 v[160:163], v165
	ds_read_b128 v[166:169], v165 offset:32
	ds_read_b128 v[0:3], v12 offset:128
	ds_read_b128 v[4:7], v12 offset:160
	ds_read_b128 v[8:11], v12 offset:192
	ds_read_b128 v[12:15], v12 offset:224
	s_waitcnt lgkmcnt(5)
	v_mfma_f32_32x32x16_f16 v[16:31], v[128:131], v[160:163], v[16:31]
	s_waitcnt lgkmcnt(0)
	v_mfma_f32_32x32x16_f16 v[0:15], v[144:147], v[160:163], v[0:15]
	v_mfma_f32_32x32x16_f16 v[16:31], v[132:135], v[166:169], v[16:31]
	v_mfma_f32_32x32x16_f16 v[0:15], v[148:151], v[166:169], v[0:15]
	ds_read_b128 v[160:163], v165 offset:64
	ds_read_b128 v[166:169], v165 offset:96
	s_waitcnt lgkmcnt(1)
	v_mfma_f32_32x32x16_f16 v[16:31], v[136:139], v[160:163], v[16:31]
	s_waitcnt lgkmcnt(0)
	v_mfma_f32_32x32x16_f16 v[16:31], v[140:143], v[166:169], v[16:31]
	v_mfma_f32_32x32x16_f16 v[0:15], v[152:155], v[160:163], v[0:15]
	s_nop 10
	v_max_f32_e32 v17, v17, v17
	v_max_f32_e32 v161, 0, v17
	v_max_f32_e32 v17, v18, v18
	v_max_f32_e32 v18, v19, v19
	v_max_f32_e32 v17, 0, v17
	v_max_f32_e32 v18, 0, v18
	v_max_f32_e32 v19, v21, v21
	v_max_f32_e32 v16, v16, v16
	v_cvt_pk_f16_f32 v17, v17, v18
	v_max_f32_e32 v18, v20, v20
	v_max_f32_e32 v20, 0, v19
	v_max_f32_e32 v19, v22, v22
	v_max_f32_e32 v21, v23, v23
	v_mfma_f32_32x32x16_f16 v[0:15], v[156:159], v[166:169], v[0:15]
	v_max_f32_e32 v16, 0, v16
	v_max_f32_e32 v18, 0, v18
	v_max_f32_e32 v19, 0, v19
	v_max_f32_e32 v21, 0, v21
	v_add_u32_e32 v160, s98, v174
	v_cvt_pk_f16_f32 v16, v16, v161
	v_cvt_pk_f16_f32 v19, v19, v21
	v_cvt_pk_f16_f32 v18, v18, v20
	ds_write2_b64 v160, v[16:17], v[18:19] offset1:2
	v_max_f32_e32 v17, v25, v25
	v_max_f32_e32 v18, 0, v17
	v_max_f32_e32 v17, v26, v26
	v_max_f32_e32 v19, v27, v27
	v_max_f32_e32 v16, v24, v24
	v_max_f32_e32 v17, 0, v17
	v_max_f32_e32 v19, 0, v19
	v_max_f32_e32 v16, 0, v16
	v_cvt_pk_f16_f32 v17, v17, v19
	v_max_f32_e32 v19, v29, v29
	v_cvt_pk_f16_f32 v16, v16, v18
	v_max_f32_e32 v18, v28, v28
	v_max_f32_e32 v20, 0, v19
	v_max_f32_e32 v19, v30, v30
	v_max_f32_e32 v21, v31, v31
	v_max_f32_e32 v18, 0, v18
	v_max_f32_e32 v19, 0, v19
	v_max_f32_e32 v21, 0, v21
	v_cvt_pk_f16_f32 v19, v19, v21
	v_cvt_pk_f16_f32 v18, v18, v20
	v_max_f32_e32 v1, v1, v1
	ds_write2_b64 v160, v[16:17], v[18:19] offset0:4 offset1:6
	v_max_f32_e32 v16, 0, v1
	v_max_f32_e32 v1, v2, v2
	v_max_f32_e32 v2, v3, v3
	v_max_f32_e32 v1, 0, v1
	v_max_f32_e32 v2, 0, v2
	v_max_f32_e32 v3, v5, v5
	v_max_f32_e32 v0, v0, v0
	v_cvt_pk_f16_f32 v1, v1, v2
	v_max_f32_e32 v2, v4, v4
	v_max_f32_e32 v4, 0, v3
	v_max_f32_e32 v3, v6, v6
	v_max_f32_e32 v5, v7, v7
	v_max_f32_e32 v0, 0, v0
	v_max_f32_e32 v2, 0, v2
	v_max_f32_e32 v3, 0, v3
	v_max_f32_e32 v5, 0, v5
	v_cvt_pk_f16_f32 v0, v0, v16
	v_cvt_pk_f16_f32 v3, v3, v5
	v_cvt_pk_f16_f32 v2, v2, v4
	ds_write2_b64 v160, v[0:1], v[2:3] offset0:8 offset1:10
	v_max_f32_e32 v1, v9, v9
	v_max_f32_e32 v2, 0, v1
	v_max_f32_e32 v1, v10, v10
	v_max_f32_e32 v3, v11, v11
	v_max_f32_e32 v0, v8, v8
	v_max_f32_e32 v1, 0, v1
	v_max_f32_e32 v3, 0, v3
	v_max_f32_e32 v0, 0, v0
	v_cvt_pk_f16_f32 v1, v1, v3
	v_max_f32_e32 v3, v13, v13
	v_cvt_pk_f16_f32 v0, v0, v2
	v_max_f32_e32 v2, v12, v12
	v_max_f32_e32 v4, 0, v3
	v_max_f32_e32 v3, v14, v14
	v_max_f32_e32 v5, v15, v15
	v_max_f32_e32 v2, 0, v2
	v_max_f32_e32 v3, 0, v3
	v_max_f32_e32 v5, 0, v5
	v_cvt_pk_f16_f32 v3, v3, v5
	v_cvt_pk_f16_f32 v2, v2, v4
	v_mad_u32_u24 v12, v195, s69, v196
	ds_write2_b64 v160, v[0:1], v[2:3] offset0:12 offset1:14
	s_waitcnt lgkmcnt(0)
	s_barrier
	v_mul_u32_u24_e32 v16, 0x410, v195
	v_add_u32_e32 v16, v196, v16
	ds_read_b128 v[8:11], v16
	ds_read_b128 v[12:15], v16 offset:16640
	ds_read_b128 v[20:23], v16 offset:64
	ds_read_b128 v[24:27], v16 offset:16704
	ds_read_b128 v[28:31], v16 offset:128
	ds_read_b128 v[160:163], v16 offset:16768
	ds_read_b128 v[164:167], v16 offset:192
	ds_read_b128 v[168:171], v16 offset:16832
	s_waitcnt lgkmcnt(7)
	v_mfma_f32_16x16x32_f16 v[0:3], v[32:35], v[8:11], 0
	ds_read_b128 v[8:11], v16 offset:256
	s_waitcnt lgkmcnt(7)
	v_mfma_f32_16x16x32_f16 v[4:7], v[32:35], v[12:15], 0
	ds_read_b128 v[12:15], v16 offset:16896
	s_waitcnt lgkmcnt(7)
	v_mfma_f32_16x16x32_f16 v[0:3], v[36:39], v[20:23], v[0:3]
	ds_read_b128 v[20:23], v16 offset:320
	s_waitcnt lgkmcnt(7)
	v_mfma_f32_16x16x32_f16 v[4:7], v[36:39], v[24:27], v[4:7]
	ds_read_b128 v[24:27], v16 offset:16960
	s_waitcnt lgkmcnt(7)
	v_mfma_f32_16x16x32_f16 v[0:3], v[40:43], v[28:31], v[0:3]
	ds_read_b128 v[28:31], v16 offset:384
	s_waitcnt lgkmcnt(7)
	v_mfma_f32_16x16x32_f16 v[4:7], v[40:43], v[160:163], v[4:7]
	ds_read_b128 v[160:163], v16 offset:17024
	s_waitcnt lgkmcnt(7)
	v_mfma_f32_16x16x32_f16 v[0:3], v[44:47], v[164:167], v[0:3]
	ds_read_b128 v[164:167], v16 offset:448
	s_waitcnt lgkmcnt(7)
	v_mfma_f32_16x16x32_f16 v[4:7], v[44:47], v[168:171], v[4:7]
	ds_read_b128 v[168:171], v16 offset:17088
	s_waitcnt lgkmcnt(7)
	v_mfma_f32_16x16x32_f16 v[0:3], v[56:59], v[8:11], v[0:3]
	ds_read_b128 v[8:11], v16 offset:512
	s_waitcnt lgkmcnt(7)
	v_mfma_f32_16x16x32_f16 v[4:7], v[56:59], v[12:15], v[4:7]
	ds_read_b128 v[12:15], v16 offset:17152
	s_waitcnt lgkmcnt(7)
	v_mfma_f32_16x16x32_f16 v[0:3], v[48:51], v[20:23], v[0:3]
	ds_read_b128 v[20:23], v16 offset:576
	s_waitcnt lgkmcnt(7)
	v_mfma_f32_16x16x32_f16 v[4:7], v[48:51], v[24:27], v[4:7]
	ds_read_b128 v[24:27], v16 offset:17216
	s_waitcnt lgkmcnt(7)
	v_mfma_f32_16x16x32_f16 v[0:3], v[52:55], v[28:31], v[0:3]
	ds_read_b128 v[28:31], v16 offset:640
	s_waitcnt lgkmcnt(7)
	v_mfma_f32_16x16x32_f16 v[4:7], v[52:55], v[160:163], v[4:7]
	ds_read_b128 v[160:163], v16 offset:17280
	s_waitcnt lgkmcnt(7)
	v_mfma_f32_16x16x32_f16 v[0:3], v[76:79], v[164:167], v[0:3]
	ds_read_b128 v[164:167], v16 offset:704
	s_waitcnt lgkmcnt(7)
	v_mfma_f32_16x16x32_f16 v[4:7], v[76:79], v[168:171], v[4:7]
	ds_read_b128 v[168:171], v16 offset:17344
	s_waitcnt lgkmcnt(7)
	v_mfma_f32_16x16x32_f16 v[0:3], v[60:63], v[8:11], v[0:3]
	ds_read_b128 v[8:11], v16 offset:768
	s_waitcnt lgkmcnt(7)
	v_mfma_f32_16x16x32_f16 v[4:7], v[60:63], v[12:15], v[4:7]
	ds_read_b128 v[12:15], v16 offset:17408
	s_waitcnt lgkmcnt(7)
	v_mfma_f32_16x16x32_f16 v[0:3], v[64:67], v[20:23], v[0:3]
	ds_read_b128 v[20:23], v16 offset:832
	s_waitcnt lgkmcnt(7)
	v_mfma_f32_16x16x32_f16 v[4:7], v[64:67], v[24:27], v[4:7]
	ds_read_b128 v[24:27], v16 offset:17472
	s_waitcnt lgkmcnt(7)
	v_mfma_f32_16x16x32_f16 v[0:3], v[68:71], v[28:31], v[0:3]
	ds_read_b128 v[28:31], v16 offset:896
	s_waitcnt lgkmcnt(7)
	v_mfma_f32_16x16x32_f16 v[4:7], v[68:71], v[160:163], v[4:7]
	ds_read_b128 v[160:163], v16 offset:17536
	s_waitcnt lgkmcnt(7)
	v_mfma_f32_16x16x32_f16 v[0:3], v[72:75], v[164:167], v[0:3]
	ds_read_b128 v[164:167], v16 offset:960
	s_waitcnt lgkmcnt(7)
	v_mfma_f32_16x16x32_f16 v[4:7], v[72:75], v[168:171], v[4:7]
	ds_read_b128 v[168:171], v16 offset:17600
	s_waitcnt lgkmcnt(7)
	v_mfma_f32_16x16x32_f16 v[0:3], v[80:83], v[8:11], v[0:3]
	s_waitcnt lgkmcnt(6)
	v_mfma_f32_16x16x32_f16 v[4:7], v[80:83], v[12:15], v[4:7]
	s_waitcnt lgkmcnt(5)
	v_mfma_f32_16x16x32_f16 v[0:3], v[84:87], v[20:23], v[0:3]
	s_waitcnt lgkmcnt(4)
	v_mfma_f32_16x16x32_f16 v[4:7], v[84:87], v[24:27], v[4:7]
	s_waitcnt lgkmcnt(3)
	v_mfma_f32_16x16x32_f16 v[0:3], v[88:91], v[28:31], v[0:3]
	s_waitcnt lgkmcnt(2)
	v_mfma_f32_16x16x32_f16 v[4:7], v[88:91], v[160:163], v[4:7]
	s_waitcnt lgkmcnt(1)
	v_mfma_f32_16x16x32_f16 v[0:3], v[92:95], v[164:167], v[0:3]
	s_waitcnt lgkmcnt(0)
	v_mfma_f32_16x16x32_f16 v[4:7], v[92:95], v[168:171], v[4:7]
	v_lshrrev_b32_e32 v17, 4, v189
	v_lshlrev_b32_e32 v17, 3, v17
	s_lshl_b32 s0, s3, 1
	v_add_u32_e32 v18, s74, v195
	v_lshl_add_u32 v17, v18, 7, v17
	v_add_u32_e32 v17, s0, v17
	v_readlane_b32 s4, v226, 0
	v_readlane_b32 s5, v226, 1
	s_mov_b32 s1, 0xc350
	v_add_u32_e32 v19, 16, v18
	v_lshlrev_b32_e32 v28, 2, v195
	s_nop 1
	v_cvt_pk_f16_f32 v20, v0, v1
	v_cvt_pk_f16_f32 v21, v2, v3
	v_cvt_pk_f16_f32 v22, v4, v5
	v_cvt_pk_f16_f32 v23, v6, v7
	v_cmp_gt_i32_e32 vcc, s1, v18
	v_cmp_gt_i32_e64 s[8:9], s1, v19
	v_mul_f32_e32 v24, v228, v0
	v_mul_f32_e32 v25, v232, v0
	v_mul_f32_e32 v26, v228, v4
	v_mul_f32_e32 v27, v232, v4
	v_fmac_f32_e32 v24, v229, v1
	v_fmac_f32_e32 v25, v233, v1
	v_fmac_f32_e32 v26, v229, v5
	v_fmac_f32_e32 v27, v233, v5
	v_fmac_f32_e32 v24, v230, v2
	v_fmac_f32_e32 v25, v234, v2
	v_fmac_f32_e32 v26, v230, v6
	v_fmac_f32_e32 v27, v234, v6
	v_fmac_f32_e32 v24, v231, v3
	v_fmac_f32_e32 v25, v235, v3
	v_fmac_f32_e32 v26, v231, v7
	v_fmac_f32_e32 v27, v235, v7
	s_mov_b64 exec, vcc
	global_store_dwordx2 v17, v[20:21], s[4:5]
	s_mov_b64 exec, s[8:9]
	global_store_dwordx2 v17, v[22:23], s[4:5] offset:2048
	s_mov_b64 exec, -1
	ds_add_f32 v28, v24 offset:54080
	ds_add_f32 v28, v25 offset:53952
	ds_add_f32 v28, v26 offset:54144
	ds_add_f32 v28, v27 offset:54016
	v_add_u32_e32 v1, s65, v189
	v_cmp_gt_i32_e32 vcc, 32, v1
	s_waitcnt lgkmcnt(0)
	s_barrier
	s_and_saveexec_b64 s[0:1], vcc
	s_cbranch_execz .LBB3_5
	v_add_u32_e32 v0, s74, v1
	s_mov_b32 s4, 0xc350
	v_lshlrev_b32_e32 v1, 2, v1
	v_cmp_gt_i32_e32 vcc, s4, v0
	v_add_u32_e32 v2, 0xd000, v1
	s_and_saveexec_b64 s[4:5], vcc
	s_cbranch_execz .LBB3_4
	ds_read2_b32 v[4:5], v2 offset0:176 offset1:208
	v_ashrrev_i32_e32 v1, 31, v0
	v_readlane_b32 s8, v226, 0
	v_lshlrev_b64 v[0:1], 2, v[0:1]
	v_readlane_b32 s10, v226, 2
	v_readlane_b32 s11, v226, 3
	v_lshl_add_u64 v[6:7], s[76:77], 0, v[0:1]
	v_readlane_b32 s9, v226, 1
	v_lshl_add_u64 v[0:1], s[10:11], 0, v[0:1]
	s_waitcnt lgkmcnt(0)
	global_store_dword v[0:1], v5, off
	global_store_dword v[6:7], v4, off
	s_branch .LBB3_4

	.amdhsa_kernel _Z8k_layer1PKiS0_PKfS2_PK15HIP_vector_typeIjLj4EEPKDv8_DF16_S9_S2_S2_S2_PDF16_PfSB_
		.amdhsa_group_segment_fixed_size 54208
		.amdhsa_private_segment_fixed_size 0
		.amdhsa_kernarg_size 360
		.amdhsa_user_sgpr_count 2
		.amdhsa_user_sgpr_dispatch_ptr 0
		.amdhsa_user_sgpr_queue_ptr 0
		.amdhsa_user_sgpr_kernarg_segment_ptr 1
		.amdhsa_user_sgpr_dispatch_id 0
		.amdhsa_user_sgpr_kernarg_preload_length 0
		.amdhsa_user_sgpr_kernarg_preload_offset 0
		.amdhsa_user_sgpr_private_segment_size 0
		.amdhsa_uses_dynamic_stack 0
		.amdhsa_enable_private_segment 0
		.amdhsa_system_sgpr_workgroup_id_x 1
		.amdhsa_system_sgpr_workgroup_id_y 0
		.amdhsa_system_sgpr_workgroup_id_z 0
		.amdhsa_system_sgpr_workgroup_info 0
		.amdhsa_system_vgpr_workitem_id 0
		.amdhsa_next_free_vgpr 236
		.amdhsa_next_free_sgpr 100
		.amdhsa_accum_offset 236
		.amdhsa_reserve_vcc 1
		.amdhsa_float_round_mode_32 0
		.amdhsa_float_round_mode_16_64 0
		.amdhsa_float_denorm_mode_32 3
		.amdhsa_float_denorm_mode_16_64 3
		.amdhsa_dx10_clamp 1
		.amdhsa_ieee_mode 1
		.amdhsa_fp16_overflow 0
		.amdhsa_tg_split 0
		.amdhsa_exception_fp_ieee_invalid_op 0
		.amdhsa_exception_fp_denorm_src 0
		.amdhsa_exception_fp_ieee_div_zero 0
		.amdhsa_exception_fp_ieee_overflow 0
		.amdhsa_exception_fp_ieee_underflow 0
		.amdhsa_exception_fp_ieee_inexact 0
		.amdhsa_exception_int_div_zero 0
	.end_amdhsa_kernel

amdhsa.kernels:
  - .agpr_count:     0
    .args:
      - .actual_access:  read_only
        .address_space:  global
        .offset:         0
        .size:           8
        .value_kind:     global_buffer
      - .actual_access:  read_only
        .address_space:  global
        .offset:         8
        .size:           8
        .value_kind:     global_buffer
      - .actual_access:  read_only
        .address_space:  global
        .offset:         16
        .size:           8
        .value_kind:     global_buffer
      - .actual_access:  read_only
        .address_space:  global
        .offset:         24
        .size:           8
        .value_kind:     global_buffer
      - .actual_access:  read_only
        .address_space:  global
        .offset:         32
        .size:           8
        .value_kind:     global_buffer
      - .actual_access:  write_only
        .address_space:  global
        .offset:         40
        .size:           8
        .value_kind:     global_buffer
      - .actual_access:  write_only
        .address_space:  global
        .offset:         48
        .size:           8
        .value_kind:     global_buffer
      - .actual_access:  write_only
        .address_space:  global
        .offset:         56
        .size:           8
        .value_kind:     global_buffer
      - .actual_access:  write_only
        .address_space:  global
        .offset:         64
        .size:           8
        .value_kind:     global_buffer
    .group_segment_fixed_size: 1024
    .kernarg_segment_align: 8
    .kernarg_segment_size: 72
    .language:       OpenCL C
    .language_version:
      - 2
      - 0
    .max_flat_workgroup_size: 512
    .name:           _Z11k_hist_prepPKiPKfS2_S2_S2_PiPfPDF16_S5_
    .private_segment_fixed_size: 0
    .sgpr_count:     20
    .sgpr_spill_count: 0
    .symbol:         _Z11k_hist_prepPKiPKfS2_S2_S2_PiPfPDF16_S5_.kd
    .uniform_work_group_size: 1
    .uses_dynamic_stack: false
    .vgpr_count:     42
    .vgpr_spill_count: 0
    .wavefront_size: 64
  - .agpr_count:     0
    .args:
      - .actual_access:  read_only
        .address_space:  global
        .offset:         0
        .size:           8
        .value_kind:     global_buffer
      - .actual_access:  read_only
        .address_space:  global
        .offset:         8
        .size:           8
        .value_kind:     global_buffer
      - .actual_access:  write_only
        .address_space:  global
        .offset:         16
        .size:           8
        .value_kind:     global_buffer
      - .actual_access:  write_only
        .address_space:  global
        .offset:         24
        .size:           8
        .value_kind:     global_buffer
      - .actual_access:  read_only
        .address_space:  global
        .offset:         32
        .size:           8
        .value_kind:     global_buffer
      - .actual_access:  read_only
        .address_space:  global
        .offset:         40
        .size:           8
        .value_kind:     global_buffer
      - .actual_access:  write_only
        .address_space:  global
        .offset:         48
        .size:           8
        .value_kind:     global_buffer
      - .actual_access:  write_only
        .address_space:  global
        .offset:         56
        .size:           8
        .value_kind:     global_buffer
      - .actual_access:  write_only
        .address_space:  global
        .offset:         64
        .size:           8
        .value_kind:     global_buffer
    .group_segment_fixed_size: 9344
    .kernarg_segment_align: 8
    .kernarg_segment_size: 72
    .language:       OpenCL C
    .language_version:
      - 2
      - 0
    .max_flat_workgroup_size: 512
    .name:           _Z14k_scatter_nodePKiS0_PjPiPKfS4_PfS5_PDF16_
    .private_segment_fixed_size: 0
    .sgpr_count:     106
    .sgpr_spill_count: 10
    .symbol:         _Z14k_scatter_nodePKiS0_PjPiPKfS4_PfS5_PDF16_.kd
    .uniform_work_group_size: 1
    .uses_dynamic_stack: false
    .vgpr_count:     118
    .vgpr_spill_count: 0
    .wavefront_size: 64
  - .agpr_count:     0
    .args:
      - .actual_access:  read_only
        .address_space:  global
        .offset:         0
        .size:           8
        .value_kind:     global_buffer
      - .actual_access:  read_only
        .address_space:  global
        .offset:         8
        .size:           8
        .value_kind:     global_buffer
      - .actual_access:  write_only
        .address_space:  global
        .offset:         16
        .size:           8
        .value_kind:     global_buffer
      - .actual_access:  write_only
        .address_space:  global
        .offset:         24
        .size:           8
        .value_kind:     global_buffer
    .group_segment_fixed_size: 3072
    .kernarg_segment_align: 8
    .kernarg_segment_size: 32
    .language:       OpenCL C
    .language_version:
      - 2
      - 0
    .max_flat_workgroup_size: 1024
    .name:           _Z5k_csrPKjPKiPiS3_
    .private_segment_fixed_size: 0
    .sgpr_count:     34
    .sgpr_spill_count: 0
    .symbol:         _Z5k_csrPKjPKiPiS3_.kd
    .uniform_work_group_size: 1
    .uses_dynamic_stack: false
    .vgpr_count:     18
    .vgpr_spill_count: 0
    .wavefront_size: 64
  - .agpr_count:     0
    .args:
      - .actual_access:  read_only
        .address_space:  global
        .offset:         0
        .size:           8
        .value_kind:     global_buffer
      - .actual_access:  read_only
        .address_space:  global
        .offset:         8
        .size:           8
        .value_kind:     global_buffer
      - .actual_access:  read_only
        .address_space:  global
        .offset:         16
        .size:           8
        .value_kind:     global_buffer
      - .actual_access:  read_only
        .address_space:  global
        .offset:         24
        .size:           8
        .value_kind:     global_buffer
      - .actual_access:  read_only
        .address_space:  global
        .offset:         32
        .size:           8
        .value_kind:     global_buffer
      - .actual_access:  read_only
        .address_space:  global
        .offset:         40
        .size:           8
        .value_kind:     global_buffer
      - .actual_access:  read_only
        .address_space:  global
        .offset:         48
        .size:           8
        .value_kind:     global_buffer
      - .actual_access:  read_only
        .address_space:  global
        .offset:         56
        .size:           8
        .value_kind:     global_buffer
      - .actual_access:  read_only
        .address_space:  global
        .offset:         64
        .size:           8
        .value_kind:     global_buffer
      - .actual_access:  read_only
        .address_space:  global
        .offset:         72
        .size:           8
        .value_kind:     global_buffer
      - .actual_access:  write_only
        .address_space:  global
        .offset:         80
        .size:           8
        .value_kind:     global_buffer
      - .actual_access:  write_only
        .address_space:  global
        .offset:         88
        .size:           8
        .value_kind:     global_buffer
      - .actual_access:  write_only
        .address_space:  global
        .offset:         96
        .size:           8
        .value_kind:     global_buffer
      - .offset:         104
        .size:           4
        .value_kind:     hidden_block_count_x
      - .offset:         108
        .size:           4
        .value_kind:     hidden_block_count_y
      - .offset:         112
        .size:           4
        .value_kind:     hidden_block_count_z
      - .offset:         116
        .size:           2
        .value_kind:     hidden_group_size_x
      - .offset:         118
        .size:           2
        .value_kind:     hidden_group_size_y
      - .offset:         120
        .size:           2
        .value_kind:     hidden_group_size_z
      - .offset:         122
        .size:           2
        .value_kind:     hidden_remainder_x
      - .offset:         124
        .size:           2
        .value_kind:     hidden_remainder_y
      - .offset:         126
        .size:           2
        .value_kind:     hidden_remainder_z
      - .offset:         144
        .size:           8
        .value_kind:     hidden_global_offset_x
      - .offset:         152
        .size:           8
        .value_kind:     hidden_global_offset_y
      - .offset:         160
        .size:           8
        .value_kind:     hidden_global_offset_z
      - .offset:         168
        .size:           2
        .value_kind:     hidden_grid_dims
    .group_segment_fixed_size: 54208
    .kernarg_segment_align: 8
    .kernarg_segment_size: 360
    .language:       OpenCL C
    .language_version:
      - 2
      - 0
    .max_flat_workgroup_size: 256
    .name:           _Z8k_layer1PKiS0_PKfS2_PK15HIP_vector_typeIjLj4EEPKDv8_DF16_S9_S2_S2_S2_PDF16_PfSB_
    .private_segment_fixed_size: 0
    .sgpr_count:     106
    .sgpr_spill_count: 7
    .symbol:         _Z8k_layer1PKiS0_PKfS2_PK15HIP_vector_typeIjLj4EEPKDv8_DF16_S9_S2_S2_S2_PDF16_PfSB_.kd
    .uniform_work_group_size: 1
    .uses_dynamic_stack: false
    .vgpr_count:     236
    .vgpr_spill_count: 0
    .wavefront_size: 64
  - .agpr_count:     0
    .args:
      - .actual_access:  read_only
        .address_space:  global
        .offset:         0
        .size:           8
        .value_kind:     global_buffer
      - .actual_access:  read_only
        .address_space:  global
        .offset:         8
        .size:           8
        .value_kind:     global_buffer
      - .actual_access:  read_only
        .address_space:  global
        .offset:         16
        .size:           8
        .value_kind:     global_buffer
      - .actual_access:  read_only
        .address_space:  global
        .offset:         24
        .size:           8
        .value_kind:     global_buffer
      - .actual_access:  read_only
        .address_space:  global
        .offset:         32
        .size:           8
        .value_kind:     global_buffer
      - .actual_access:  read_only
        .address_space:  global
        .offset:         40
        .size:           8
        .value_kind:     global_buffer
      - .actual_access:  write_only
        .address_space:  global
        .offset:         48
        .size:           8
        .value_kind:     global_buffer
    .group_segment_fixed_size: 0
    .kernarg_segment_align: 8
    .kernarg_segment_size: 56
    .language:       OpenCL C
    .language_version:
      - 2
      - 0
    .max_flat_workgroup_size: 256
    .name:           _Z8k_layer2PKiS0_PKfS2_PK15HIP_vector_typeIjLj4EES2_Pf
    .private_segment_fixed_size: 0
    .sgpr_count:     52
    .sgpr_spill_count: 0
    .symbol:         _Z8k_layer2PKiS0_PKfS2_PK15HIP_vector_typeIjLj4EES2_Pf.kd
    .uniform_work_group_size: 1
    .uses_dynamic_stack: false
    .vgpr_count:     70
    .vgpr_spill_count: 0
    .wavefront_size: 64
